# grid barrier: the 16th-from-last arriver of each XCD starts an early L2 write-back (off the critical path) ahead of the leader's release write-back
# baseline (speedup 1.0000x reference)
.LBB0_236:
	s_or_b64 exec, exec, s[8:9]
	v_cvt_f32_u32_e32 v5, v3
	s_waitcnt vmcnt(0)
	v_readfirstlane_b32 s2, v4
	v_sub_u32_e32 v4, 0, v3
	v_rcp_iflag_f32_e32 v5, v5
	v_add_u32_e32 v6, s2, v2
	v_mul_f32_e32 v5, 0x4f7ffffe, v5
	v_cvt_u32_f32_e32 v5, v5
	v_mul_lo_u32 v2, v4, v5
	v_mul_hi_u32 v2, v5, v2
	v_add_u32_e32 v2, v5, v2
	v_mul_hi_u32 v2, v6, v2
	v_mul_lo_u32 v4, v2, v3
	v_sub_u32_e32 v4, v6, v4
	v_add_u32_e32 v5, 1, v2
	v_cmp_ge_u32_e32 vcc, v4, v3
	s_nop 1
	v_cndmask_b32_e32 v2, v2, v5, vcc
	v_sub_u32_e32 v5, v4, v3
	v_cndmask_b32_e32 v4, v4, v5, vcc
	v_add_u32_e32 v5, 1, v2
	v_cmp_ge_u32_e32 vcc, v4, v3
	v_add_u32_e32 v4, 1, v6
	s_nop 0
	v_cndmask_b32_e32 v2, v2, v5, vcc
	v_mul_lo_u32 v5, v3, v2
	v_add_u32_e32 v3, v5, v3
	v_cmp_ne_u32_e32 vcc, v4, v3
	s_and_saveexec_b64 s[2:3], vcc
	s_xor_b64 s[6:7], exec, s[2:3]
	s_cbranch_execz .LBB0_252
	s_waitcnt lgkmcnt(0)
	v_add_u32_e32 v5, 16, v4
	v_cmp_ne_u32_e32 vcc, v5, v3
	s_cbranch_vccnz .Lmy_nowb_0
	buffer_wbl2 sc1
.Lmy_nowb_0:
	v_mov_b32_e32 v1, 0x7500
	global_load_dword v1, v1, s[84:85] sc1
	s_add_u32 s12, s84, 0x7500
	s_addc_u32 s13, s85, 0
	s_waitcnt vmcnt(0)
	v_cmp_eq_u32_e32 vcc, v1, v2
	s_and_saveexec_b64 s[8:9], vcc
	s_cbranch_execz .LBB0_251
	s_add_u32 s10, s84, 0x4200
	s_addc_u32 s11, s85, 0
	s_mov_b32 s2, 1
	s_mov_b64 s[14:15], 0
	v_mov_b32_e32 v1, 0
	s_branch .LBB0_240

.LBB0_784:
	s_or_b64 exec, exec, s[10:11]
	v_cvt_f32_u32_e32 v5, v3
	s_waitcnt vmcnt(0)
	v_readfirstlane_b32 s8, v4
	v_sub_u32_e32 v4, 0, v3
	v_rcp_iflag_f32_e32 v5, v5
	v_add_u32_e32 v6, s8, v2
	v_mul_f32_e32 v5, 0x4f7ffffe, v5
	v_cvt_u32_f32_e32 v5, v5
	v_mul_lo_u32 v2, v4, v5
	v_mul_hi_u32 v2, v5, v2
	v_add_u32_e32 v2, v5, v2
	v_mul_hi_u32 v2, v6, v2
	v_mul_lo_u32 v4, v2, v3
	v_sub_u32_e32 v4, v6, v4
	v_add_u32_e32 v5, 1, v2
	v_cmp_ge_u32_e32 vcc, v4, v3
	s_nop 1
	v_cndmask_b32_e32 v2, v2, v5, vcc
	v_sub_u32_e32 v5, v4, v3
	v_cndmask_b32_e32 v4, v4, v5, vcc
	v_add_u32_e32 v5, 1, v2
	v_cmp_ge_u32_e32 vcc, v4, v3
	v_add_u32_e32 v4, 1, v6
	s_nop 0
	v_cndmask_b32_e32 v2, v2, v5, vcc
	v_mul_lo_u32 v5, v3, v2
	v_add_u32_e32 v3, v5, v3
	v_cmp_ne_u32_e32 vcc, v4, v3
	s_and_saveexec_b64 s[8:9], vcc
	s_xor_b64 s[8:9], exec, s[8:9]
	s_cbranch_execz .LBB0_798
	s_waitcnt lgkmcnt(0)
	v_add_u32_e32 v5, 16, v4
	v_cmp_ne_u32_e32 vcc, v5, v3
	s_cbranch_vccnz .Lmy_nowb_2
	buffer_wbl2 sc1
.Lmy_nowb_2:
	v_mov_b32_e32 v1, 0x7500
	global_load_dword v1, v1, s[84:85] sc1
	s_add_u32 s14, s84, 0x7500
	s_addc_u32 s15, s85, 0
	s_waitcnt vmcnt(0)
	v_cmp_eq_u32_e32 vcc, v1, v2
	s_and_saveexec_b64 s[10:11], vcc
	s_cbranch_execz .LBB0_797
	s_add_u32 s12, s84, 0x4200
	s_addc_u32 s13, s85, 0
	s_mov_b32 s26, 1
	s_mov_b64 s[16:17], 0
	v_mov_b32_e32 v1, 0
	s_branch .LBB0_788

.LBB0_952:
	s_or_b64 exec, exec, s[8:9]
	v_cvt_f32_u32_e32 v5, v3
	s_waitcnt vmcnt(0)
	v_readfirstlane_b32 s6, v4
	v_sub_u32_e32 v4, 0, v3
	v_rcp_iflag_f32_e32 v5, v5
	v_add_u32_e32 v6, s6, v2
	v_mul_f32_e32 v5, 0x4f7ffffe, v5
	v_cvt_u32_f32_e32 v5, v5
	v_mul_lo_u32 v2, v4, v5
	v_mul_hi_u32 v2, v5, v2
	v_add_u32_e32 v2, v5, v2
	v_mul_hi_u32 v2, v6, v2
	v_mul_lo_u32 v4, v2, v3
	v_sub_u32_e32 v4, v6, v4
	v_add_u32_e32 v5, 1, v2
	v_cmp_ge_u32_e32 vcc, v4, v3
	s_nop 1
	v_cndmask_b32_e32 v2, v2, v5, vcc
	v_sub_u32_e32 v5, v4, v3
	v_cndmask_b32_e32 v4, v4, v5, vcc
	v_add_u32_e32 v5, 1, v2
	v_cmp_ge_u32_e32 vcc, v4, v3
	v_add_u32_e32 v4, 1, v6
	s_nop 0
	v_cndmask_b32_e32 v2, v2, v5, vcc
	v_mul_lo_u32 v5, v3, v2
	v_add_u32_e32 v3, v5, v3
	v_cmp_ne_u32_e32 vcc, v4, v3
	s_and_saveexec_b64 s[6:7], vcc
	s_xor_b64 s[6:7], exec, s[6:7]
	s_cbranch_execz .LBB0_966
	s_waitcnt lgkmcnt(0)
	v_add_u32_e32 v5, 16, v4
	v_cmp_ne_u32_e32 vcc, v5, v3
	s_cbranch_vccnz .Lmy_nowb_4
	buffer_wbl2 sc1
.Lmy_nowb_4:
	v_mov_b32_e32 v1, 0x7500
	global_load_dword v1, v1, s[84:85] sc1
	s_add_u32 s12, s84, 0x7500
	s_addc_u32 s13, s85, 0
	s_waitcnt vmcnt(0)
	v_cmp_eq_u32_e32 vcc, v1, v2
	s_and_saveexec_b64 s[8:9], vcc
	s_cbranch_execz .LBB0_965
	s_add_u32 s10, s84, 0x4200
	s_addc_u32 s11, s85, 0
	s_mov_b32 s24, 1
	s_mov_b64 s[14:15], 0
	v_mov_b32_e32 v1, 0
	s_branch .LBB0_956

.LBB0_1130:
	s_or_b64 exec, exec, s[12:13]
	v_cvt_f32_u32_e32 v5, v3
	s_waitcnt vmcnt(0)
	v_readfirstlane_b32 s10, v4
	v_sub_u32_e32 v4, 0, v3
	v_rcp_iflag_f32_e32 v5, v5
	v_add_u32_e32 v6, s10, v2
	v_mul_f32_e32 v5, 0x4f7ffffe, v5
	v_cvt_u32_f32_e32 v5, v5
	v_mul_lo_u32 v2, v4, v5
	v_mul_hi_u32 v2, v5, v2
	v_add_u32_e32 v2, v5, v2
	v_mul_hi_u32 v2, v6, v2
	v_mul_lo_u32 v4, v2, v3
	v_sub_u32_e32 v4, v6, v4
	v_add_u32_e32 v5, 1, v2
	v_cmp_ge_u32_e32 vcc, v4, v3
	s_nop 1
	v_cndmask_b32_e32 v2, v2, v5, vcc
	v_sub_u32_e32 v5, v4, v3
	v_cndmask_b32_e32 v4, v4, v5, vcc
	v_add_u32_e32 v5, 1, v2
	v_cmp_ge_u32_e32 vcc, v4, v3
	v_add_u32_e32 v4, 1, v6
	s_nop 0
	v_cndmask_b32_e32 v2, v2, v5, vcc
	v_mul_lo_u32 v5, v3, v2
	v_add_u32_e32 v3, v5, v3
	v_cmp_ne_u32_e32 vcc, v4, v3
	s_and_saveexec_b64 s[10:11], vcc
	s_xor_b64 s[10:11], exec, s[10:11]
	s_cbranch_execz .LBB0_1144
	s_waitcnt lgkmcnt(0)
	v_add_u32_e32 v5, 16, v4
	v_cmp_ne_u32_e32 vcc, v5, v3
	s_cbranch_vccnz .Lmy_nowb_6
	buffer_wbl2 sc1
.Lmy_nowb_6:
	v_mov_b32_e32 v1, 0x7500
	global_load_dword v1, v1, s[84:85] sc1
	s_add_u32 s16, s84, 0x7500
	s_addc_u32 s17, s85, 0
	s_waitcnt vmcnt(0)
	v_cmp_eq_u32_e32 vcc, v1, v2
	s_and_saveexec_b64 s[12:13], vcc
	s_cbranch_execz .LBB0_1143
	s_add_u32 s14, s84, 0x4200
	s_addc_u32 s15, s85, 0
	s_mov_b32 s28, 1
	s_mov_b64 s[18:19], 0
	v_mov_b32_e32 v1, 0
	s_branch .LBB0_1134

.Lmy_nowb_7:
	v_mov_b32_e32 v1, 0x7500
	global_load_dword v1, v1, s[84:85] sc1
	s_add_u32 s12, s84, 0x7500
	s_addc_u32 s13, s85, 0
	s_waitcnt vmcnt(0)
	v_cmp_eq_u32_e32 vcc, v1, v2
	s_and_saveexec_b64 s[8:9], vcc
	s_cbranch_execz .LBB0_1297
	s_add_u32 s10, s84, 0x4200
	s_addc_u32 s11, s85, 0
	s_mov_b32 s26, 1
	s_mov_b64 s[14:15], 0
	v_mov_b32_e32 v1, 0
	s_branch .LBB0_1288
